# speedup vs baseline: 1.0476x; 1.0108x over previous
_Z6k_gemmPKfS0_PK15HIP_vector_typeIjLj4EEPDF16_PKh:
	s_load_dwordx4 s[20:23], s[0:1], 0x0
	s_load_dwordx4 s[4:7], s[0:1], 0x10
	s_load_dwordx2 s[38:39], s[0:1], 0x20
	v_readfirstlane_b32 s8, v0
	v_and_b32_e32 v1, 63, v0
	s_nop 3
	s_lshr_b32 s8, s8, 6
	s_and_b32 s40, s2, 7
	s_lshr_b32 s41, s2, 3
	s_mul_i32 s18, s40, 0x187
	s_min_u32 s19, s18, 0xaae
	s_add_i32 s18, s18, s41
	s_sub_i32 s33, s19, s18
	s_addk_i32 s33, 0x1c6
	s_ashr_i32 s9, s33, 6
	s_max_i32 s9, s9, 0
	s_cmp_eq_u32 s9, 0
	s_cbranch_scc1 .Lg_end
	s_add_i32 s11, s9, 4
	s_lshl_b32 s18, s18, 4
	s_lshl_b32 s19, s8, 2
	s_add_i32 s33, s18, s19
	s_mul_i32 s12, s33, 0x4b0
	s_lshl_b32 s32, s18, 8
	s_sub_u32 s32, s32, 0x100000
	s_mov_b32 s10, 0
	v_lshl_add_u32 v253, v1, 10, s33
	v_mov_b32_e32 v247, 0
	v_cmp_gt_i32_e32 vcc, s9, v1
	s_mov_b32 s18, 0xc350
	v_cmp_gt_i32_e64 s[36:37], s18, v253
	s_and_b64 vcc, vcc, s[36:37]
	s_waitcnt lgkmcnt(0)
	s_and_saveexec_b64 s[36:37], vcc
	global_load_dword v247, v253, s[38:39]
	s_mov_b64 exec, s[36:37]
	s_mov_b32 s24, s22
	s_and_b32 s25, s23, 0xffff
	s_mov_b32 s26, 0x3938700
	s_mov_b32 s27, 0x20000
	s_and_b32 s21, s21, 0xffff
	s_mov_b32 s22, 0x3938700
	s_mov_b32 s23, 0x20000
	s_mov_b32 s28, s6
	s_and_b32 s29, s7, 0xffff
	s_mov_b32 s30, 0xc35000
	s_mov_b32 s31, 0x20000
	v_lshlrev_b32_e32 v238, 4, v1
	v_mul_u32_u24_e32 v253, 0x1746, v1
	v_lshrrev_b32_e32 v253, 16, v253
	v_min_u32_e32 v253, 3, v253
	v_mul_u32_u24_e32 v254, 11, v253
	v_sub_u32_e32 v254, v1, v254
	v_lshlrev_b32_e32 v240, 3, v253
	v_mul_u32_u24_e32 v249, 0x4b0, v253
	v_lshl_add_u32 v249, v254, 4, v249
	v_add_u32_e32 v249, 0x400, v249
	v_mov_b32_e32 v255, 0x80000000
	v_cmp_gt_u32_e64 s[34:35], 44, v1
	s_nop 1
	v_cndmask_b32_e64 v239, v255, v249, s[34:35]
	v_lshl_add_u32 v250, s8, 2, v253
	v_mul_u32_u24_e32 v250, 0x4e0, v250
	v_lshl_add_u32 v250, v254, 3, v250
	v_add_u32_e32 v242, 0x200, v250
	s_mul_i32 s18, s8, 0x1380
	v_lshl_add_u32 v241, v1, 3, s18
	v_and_b32_e32 v249, 15, v1
	v_lshrrev_b32_e32 v250, 4, v1
	v_mul_u32_u24_e32 v243, 0x4e0, v249
	v_lshl_add_u32 v243, v250, 4, v243
	v_mul_u32_u24_e32 v244, 0x440, v250
	v_lshl_add_u32 v244, v249, 1, v244
	s_lshl_b32 s18, s8, 6
	s_add_i32 s18, s18, 39936
	v_add_u32_e32 v244, s18, v244
	v_lshrrev_b32_e32 v249, 4, v0
	v_and_b32_e32 v250, 15, v0
	v_mul_u32_u24_e32 v245, 0x110, v249
	v_lshl_add_u32 v245, v250, 4, v245
	v_add_u32_e32 v245, 39936, v245
	v_lshlrev_b32_e32 v246, 8, v249
	v_lshl_add_u32 v246, v250, 4, v246
	s_lshl_b32 s18, s8, 12
	s_add_i32 s18, s18, 48640
	v_lshl_add_u32 v248, v1, 4, s18
	v_cmp_gt_u32_e32 vcc, 32, v0
	s_and_saveexec_b64 s[36:37], vcc
	v_mul_u32_u24_e32 v251, 0x4e00, v249
	v_mul_u32_u24_e32 v252, 0x4e0, v250
	v_add_u32_e32 v254, v251, v252
	v_mov_b32_e32 v250, 0
	v_mov_b32_e32 v251, 0
	v_mov_b32_e32 v252, 0
	v_mov_b32_e32 v253, 0
	ds_write_b128 v254, v[250:253] offset:1200
	s_mov_b64 exec, s[36:37]
	s_lshl_b32 s18, s8, 11
	v_lshl_add_u32 v253, v1, 4, s18
	v_add_u32_e32 v254, 0x22000, v253
	global_load_dwordx4 v[178:181], v254, s[4:5]
	global_load_dwordx4 v[182:185], v254, s[4:5] offset:1024
	v_add_u32_e32 v254, 0x2000, v254
	global_load_dwordx4 v[186:189], v254, s[4:5]
	global_load_dwordx4 v[190:193], v254, s[4:5] offset:1024
	v_mov_b32_e32 v236, v253
	s_waitcnt vmcnt(4)
	v_readlane_b32 s13, v247, s10
	s_add_u32 s14, s12, 0x4b0
	s_add_u32 s15, s12, 0x960
	s_add_u32 s16, s12, 0xe10
	s_nop 1
	s_and_b32 s18, s13, 0xff
	s_cmp_eq_u32 s18, 1
	s_cselect_b32 s42, s12, 0x80000000
	s_and_b32 s18, s13, 0xff00
	s_cmp_eq_u32 s18, 0x100
	s_cselect_b32 s14, s14, 0x80000000
	s_and_b32 s18, s13, 0xff0000
	s_cmp_eq_u32 s18, 0x10000
	s_cselect_b32 s15, s15, 0x80000000
	s_and_b32 s18, s13, 0xff000000
	s_cmp_eq_u32 s18, 0x1000000
	s_cselect_b32 s16, s16, 0x80000000
	v_lshrrev_b32_e64 v253, v240, s13
	v_and_b32_e32 v253, 0xff, v253
	v_cmp_eq_u32_e32 vcc, 1, v253
	s_nop 1
	v_cndmask_b32_e32 v254, v255, v239, vcc
	buffer_load_dwordx4 v[138:141], v238, s[20:23], s42 offen nt
	buffer_load_dwordx4 v[142:145], v238, s[24:27], s42 offen nt
	buffer_load_dwordx4 v[146:149], v238, s[20:23], s14 offen nt
	buffer_load_dwordx4 v[150:153], v238, s[24:27], s14 offen nt
	buffer_load_dwordx4 v[154:157], v238, s[20:23], s15 offen nt
	buffer_load_dwordx4 v[158:161], v238, s[24:27], s15 offen nt
	buffer_load_dwordx4 v[162:165], v238, s[20:23], s16 offen nt
	buffer_load_dwordx4 v[166:169], v238, s[24:27], s16 offen nt
	buffer_load_dwordx4 v[170:173], v254, s[20:23], s12 offen nt
	buffer_load_dwordx4 v[174:177], v254, s[24:27], s12 offen nt
	s_add_u32 s12, s12, 0x12c000
	s_add_u32 s32, s32, 0x40000
	s_mov_b32 s19, 0x80000000
	buffer_store_dwordx4 v[226:229], v246, s[28:31], s19 offen nt
	s_mov_b32 s10, 1
	global_load_dwordx4 v[2:5], v236, s[4:5]
	global_load_dwordx4 v[6:9], v236, s[4:5] offset:1024
	v_add_u32_e32 v236, 0x2000, v236
	global_load_dwordx4 v[10:13], v236, s[4:5]
	global_load_dwordx4 v[14:17], v236, s[4:5] offset:1024
	v_add_u32_e32 v236, 0x2000, v236
	global_load_dwordx4 v[18:21], v236, s[4:5]
	global_load_dwordx4 v[22:25], v236, s[4:5] offset:1024
	v_add_u32_e32 v236, 0x2000, v236
	global_load_dwordx4 v[26:29], v236, s[4:5]
	global_load_dwordx4 v[30:33], v236, s[4:5] offset:1024
	v_add_u32_e32 v236, 0x2000, v236
	global_load_dwordx4 v[34:37], v236, s[4:5]
	global_load_dwordx4 v[38:41], v236, s[4:5] offset:1024
	v_add_u32_e32 v236, 0x2000, v236
	global_load_dwordx4 v[42:45], v236, s[4:5]
	global_load_dwordx4 v[46:49], v236, s[4:5] offset:1024
	v_add_u32_e32 v236, 0x2000, v236
	global_load_dwordx4 v[50:53], v236, s[4:5]
	global_load_dwordx4 v[54:57], v236, s[4:5] offset:1024
	v_add_u32_e32 v236, 0x2000, v236
	global_load_dwordx4 v[58:61], v236, s[4:5]
	global_load_dwordx4 v[62:65], v236, s[4:5] offset:1024
	v_add_u32_e32 v236, 0x2000, v236
	global_load_dwordx4 v[66:69], v236, s[4:5]
	global_load_dwordx4 v[70:73], v236, s[4:5] offset:1024
	v_add_u32_e32 v236, 0x2000, v236
	global_load_dwordx4 v[74:77], v236, s[4:5]
	global_load_dwordx4 v[78:81], v236, s[4:5] offset:1024
	v_add_u32_e32 v236, 0x2000, v236
	global_load_dwordx4 v[82:85], v236, s[4:5]
	global_load_dwordx4 v[86:89], v236, s[4:5] offset:1024
	v_add_u32_e32 v236, 0x2000, v236
	global_load_dwordx4 v[90:93], v236, s[4:5]
	global_load_dwordx4 v[94:97], v236, s[4:5] offset:1024
	v_add_u32_e32 v236, 0x2000, v236
	global_load_dwordx4 v[98:101], v236, s[4:5]
	global_load_dwordx4 v[102:105], v236, s[4:5] offset:1024
	v_add_u32_e32 v236, 0x2000, v236
	global_load_dwordx4 v[106:109], v236, s[4:5]
	global_load_dwordx4 v[110:113], v236, s[4:5] offset:1024
	v_add_u32_e32 v236, 0x2000, v236
	global_load_dwordx4 v[114:117], v236, s[4:5]
	global_load_dwordx4 v[118:121], v236, s[4:5] offset:1024
	v_add_u32_e32 v236, 0x2000, v236
	global_load_dwordx4 v[122:125], v236, s[4:5]
	global_load_dwordx4 v[126:129], v236, s[4:5] offset:1024
	v_add_u32_e32 v236, 0x2000, v236
	global_load_dwordx4 v[130:133], v236, s[4:5]
	global_load_dwordx4 v[134:137], v236, s[4:5] offset:1024
	s_waitcnt vmcnt(45)
	ds_write_b128 v248, v[178:181]
	ds_write_b128 v248, v[182:185] offset:1024
	ds_write_b128 v248, v[186:189] offset:2048
	ds_write_b128 v248, v[190:193] offset:3072
	s_waitcnt lgkmcnt(0)
	s_barrier
	s_branch .Lg_half1

_Z6k_poolPKDF16_PKiS2_PKfS4_S4_Pf:
	s_load_dwordx8 s[4:11], s[0:1], 0x0
	s_load_dwordx4 s[20:23], s[0:1], 0x28
	v_mov_b32_e32 v61, 0
	s_ashr_i32 s3, s2, 31
	s_lshl_b64 s[12:13], s[2:3], 2
	v_lshrrev_b32_e32 v37, 4, v0
	v_bfe_u32 v1, v0, 3, 1
	s_waitcnt lgkmcnt(0)
	s_add_u32 s6, s6, s12
	s_addc_u32 s7, s7, s13
	s_lshl_b32 s12, s2, 9
	s_ashr_i32 s13, s12, 31
	s_lshl_b64 s[12:13], s[12:13], 2
	s_add_u32 s8, s8, s12
	v_add_u32_e32 v1, v1, v37
	s_addc_u32 s9, s9, s13
	v_lshlrev_b32_e32 v3, 2, v1
	global_load_dword v2, v3, s[8:9]
	global_load_dword v4, v3, s[8:9] offset:256
	global_load_dword v10, v3, s[8:9] offset:512
	global_load_dword v14, v3, s[8:9] offset:768
	global_load_dword v18, v3, s[8:9] offset:1024
	global_load_dword v24, v3, s[8:9] offset:1280
	v_min_u32_e32 v1, 63, v1
	v_lshlrev_b32_e32 v1, 2, v1
	global_load_dword v6, v3, s[8:9] offset:1536
	global_load_dword v8, v1, s[8:9] offset:1792
	v_and_b32_e32 v36, 15, v0
	v_mov_b32_e32 v13, 0
	v_lshlrev_b32_e32 v12, 4, v36
	v_lshl_add_u64 v[22:23], s[4:5], 0, v[12:13]
	v_mbcnt_lo_u32_b32 v1, -1, 0
	s_load_dwordx2 s[4:5], s[0:1], 0x20
	v_mbcnt_hi_u32_b32 v1, -1, v1
	v_and_b32_e32 v38, 63, v0
	v_and_b32_e32 v9, 56, v1
	v_lshlrev_b32_e32 v7, 2, v38
	v_cmp_eq_u32_e32 vcc, 56, v9
	s_load_dword s6, s[6:7], 0x0
	v_mov_b32_e32 v40, 0xfc00fc00
	v_cndmask_b32_e64 v9, 8, 0, vcc
	v_add_lshl_u32 v49, v9, v1, 2
	v_or_b32_e32 v41, 64, v37
	v_or_b32_e32 v46, 0x80, v37
	s_mov_b32 s3, 0xfc00
	v_or_b32_e32 v47, 0xc0, v37
	v_or_b32_e32 v48, 0x100, v37
	s_waitcnt vmcnt(7)
	v_ashrrev_i32_e32 v3, 31, v2
	v_lshlrev_b64 v[2:3], 8, v[2:3]
	v_lshl_add_u64 v[2:3], v[22:23], 0, v[2:3]
	s_waitcnt vmcnt(6)
	v_ashrrev_i32_e32 v5, 31, v4
	global_load_dwordx4 v[30:33], v[2:3], off
	v_lshlrev_b64 v[2:3], 8, v[4:5]
	v_lshl_add_u64 v[2:3], v[22:23], 0, v[2:3]
	s_waitcnt vmcnt(6)
	v_ashrrev_i32_e32 v11, 31, v10
	global_load_dwordx4 v[26:29], v[2:3], off
	v_lshlrev_b64 v[2:3], 8, v[10:11]
	v_lshl_add_u64 v[2:3], v[22:23], 0, v[2:3]
	s_waitcnt vmcnt(6)
	v_ashrrev_i32_e32 v15, 31, v14
	global_load_dwordx4 v[10:13], v[2:3], off
	v_lshlrev_b64 v[2:3], 8, v[14:15]
	v_lshl_add_u64 v[2:3], v[22:23], 0, v[2:3]
	s_waitcnt vmcnt(6)
	v_ashrrev_i32_e32 v19, 31, v18
	global_load_dwordx4 v[14:17], v[2:3], off
	v_lshlrev_b64 v[2:3], 8, v[18:19]
	v_lshl_add_u64 v[2:3], v[22:23], 0, v[2:3]
	s_waitcnt vmcnt(6)
	v_ashrrev_i32_e32 v25, 31, v24
	global_load_dwordx4 v[18:21], v[2:3], off
	v_lshlrev_b64 v[2:3], 8, v[24:25]
	v_lshl_add_u64 v[2:3], v[22:23], 0, v[2:3]
	global_load_dwordx4 v[2:5], v[2:3], off
	s_nop 0
	global_load_dword v39, v7, s[10:11]
	s_waitcnt lgkmcnt(0)
	global_load_dword v34, v7, s[4:5]
	global_load_dword v35, v7, s[4:5] offset:256
	s_waitcnt vmcnt(10)
	v_ashrrev_i32_e32 v7, 31, v6
	s_waitcnt vmcnt(9)
	v_ashrrev_i32_e32 v9, 31, v8
	v_lshlrev_b64 v[6:7], 8, v[6:7]
	v_lshlrev_b64 v[8:9], 8, v[8:9]
	v_lshl_add_u64 v[42:43], v[22:23], 0, v[6:7]
	v_lshl_add_u64 v[44:45], v[22:23], 0, v[8:9]
	global_load_dwordx4 v[22:25], v[42:43], off
	global_load_dwordx4 v[6:9], v[44:45], off
	global_load_dwordx2 v[62:63], v61, s[20:21]
	s_min_i32 s4, s6, 0x1ff
	v_cmp_gt_i32_e32 vcc, s4, v37
	s_waitcnt vmcnt(10)
	ds_bpermute_b32 v42, v49, v30
	ds_bpermute_b32 v43, v49, v31
	ds_bpermute_b32 v44, v49, v32
	ds_bpermute_b32 v45, v49, v33
	s_waitcnt vmcnt(9)
	ds_bpermute_b32 v50, v49, v26
	ds_bpermute_b32 v51, v49, v27
	ds_bpermute_b32 v52, v49, v28
	ds_bpermute_b32 v53, v49, v29
	s_waitcnt vmcnt(8)
	ds_bpermute_b32 v54, v49, v10
	ds_bpermute_b32 v55, v49, v11
	ds_bpermute_b32 v56, v49, v12
	ds_bpermute_b32 v57, v49, v13
	s_waitcnt vmcnt(7)
	ds_bpermute_b32 v58, v49, v14
	ds_bpermute_b32 v59, v49, v15
	s_waitcnt lgkmcnt(13)
	v_pk_add_f16 v30, v30, v42
	s_waitcnt lgkmcnt(12)
	v_pk_add_f16 v31, v31, v43
	s_waitcnt lgkmcnt(11)
	v_pk_add_f16 v32, v32, v44
	s_waitcnt lgkmcnt(10)
	v_pk_add_f16 v33, v33, v45
	ds_bpermute_b32 v42, v49, v16
	ds_bpermute_b32 v43, v49, v17
	s_waitcnt vmcnt(6)
	ds_bpermute_b32 v44, v49, v18
	ds_bpermute_b32 v45, v49, v19
	s_waitcnt lgkmcnt(13)
	v_pk_add_f16 v26, v26, v50
	s_waitcnt lgkmcnt(12)
	v_pk_add_f16 v27, v27, v51
	s_waitcnt lgkmcnt(11)
	v_pk_add_f16 v28, v28, v52
	s_waitcnt lgkmcnt(10)
	v_pk_add_f16 v29, v29, v53
	ds_bpermute_b32 v50, v49, v20
	ds_bpermute_b32 v51, v49, v21
	v_cndmask_b32_e32 v30, v40, v30, vcc
	v_cndmask_b32_e32 v31, v40, v31, vcc
	v_cndmask_b32_e32 v32, v40, v32, vcc
	v_cndmask_b32_e32 v33, v40, v33, vcc
	v_cmp_gt_i32_e32 vcc, s4, v41
	s_waitcnt vmcnt(5)
	ds_bpermute_b32 v52, v49, v2
	s_waitcnt lgkmcnt(12)
	v_pk_add_f16 v10, v10, v54
	s_waitcnt lgkmcnt(11)
	v_pk_add_f16 v11, v11, v55
	s_waitcnt lgkmcnt(10)
	v_pk_add_f16 v12, v12, v56
	s_waitcnt lgkmcnt(9)
	v_pk_add_f16 v13, v13, v57
	v_cndmask_b32_e32 v26, v40, v26, vcc
	v_cndmask_b32_e32 v27, v40, v27, vcc
	v_cndmask_b32_e32 v28, v40, v28, vcc
	v_cndmask_b32_e32 v29, v40, v29, vcc
	v_cmp_gt_i32_e32 vcc, s4, v46
	v_pk_max_f16 v30, v30, v30
	v_pk_max_f16 v31, v31, v31
	s_waitcnt lgkmcnt(8)
	v_pk_add_f16 v14, v14, v58
	s_waitcnt lgkmcnt(7)
	v_pk_add_f16 v15, v15, v59
	v_cndmask_b32_e32 v10, v40, v10, vcc
	v_cndmask_b32_e32 v11, v40, v11, vcc
	v_cndmask_b32_e32 v12, v40, v12, vcc
	v_cndmask_b32_e32 v13, v40, v13, vcc
	v_cmp_gt_i32_e32 vcc, s4, v47
	v_pk_max_f16 v26, v26, v26
	v_pk_max_f16 v27, v27, v27
	v_pk_max_f16 v30, v30, s3 op_sel_hi:[1,0]
	v_pk_max_f16 v31, v31, s3 op_sel_hi:[1,0]
	v_cndmask_b32_e32 v14, v40, v14, vcc
	v_cndmask_b32_e32 v15, v40, v15, vcc
	v_pk_max_f16 v10, v10, v10
	v_pk_max_f16 v11, v11, v11
	v_pk_max_f16 v26, v30, v26
	v_pk_max_f16 v27, v31, v27
	s_waitcnt lgkmcnt(6)
	v_pk_add_f16 v16, v16, v42
	s_waitcnt lgkmcnt(5)
	v_pk_add_f16 v17, v17, v43
	v_pk_max_f16 v14, v14, v14
	v_pk_max_f16 v15, v15, v15
	v_pk_max_f16 v10, v26, v10
	v_pk_max_f16 v11, v27, v11
	s_waitcnt lgkmcnt(4)
	v_pk_add_f16 v18, v18, v44
	s_waitcnt lgkmcnt(3)
	v_pk_add_f16 v19, v19, v45
	s_waitcnt lgkmcnt(2)
	v_pk_add_f16 v20, v20, v50
	s_waitcnt lgkmcnt(1)
	v_pk_add_f16 v21, v21, v51
	v_cndmask_b32_e32 v16, v40, v16, vcc
	v_cndmask_b32_e32 v17, v40, v17, vcc
	v_cmp_gt_i32_e32 vcc, s4, v48
	v_pk_max_f16 v10, v10, v14
	v_pk_max_f16 v11, v11, v15
	v_or_b32_e32 v14, 0x140, v37
	ds_bpermute_b32 v15, v49, v3
	v_cndmask_b32_e32 v18, v40, v18, vcc
	v_cndmask_b32_e32 v19, v40, v19, vcc
	v_cndmask_b32_e32 v20, v40, v20, vcc
	v_cndmask_b32_e32 v21, v40, v21, vcc
	s_waitcnt lgkmcnt(1)
	v_pk_add_f16 v2, v2, v52
	v_cmp_gt_i32_e32 vcc, s4, v14
	v_pk_max_f16 v18, v18, v18
	s_waitcnt lgkmcnt(0)
	v_pk_add_f16 v3, v3, v15
	v_cndmask_b32_e32 v2, v40, v2, vcc
	v_pk_max_f16 v10, v10, v18
	v_pk_max_f16 v2, v2, v2
	v_pk_max_f16 v32, v32, v32
	v_pk_max_f16 v2, v10, v2
	ds_bpermute_b32 v10, v49, v4
	v_pk_max_f16 v19, v19, v19
	v_cndmask_b32_e32 v3, v40, v3, vcc
	v_pk_max_f16 v28, v28, v28
	v_pk_max_f16 v32, v32, s3 op_sel_hi:[1,0]
	v_pk_max_f16 v11, v11, v19
	v_pk_max_f16 v3, v3, v3
	v_pk_max_f16 v12, v12, v12
	v_pk_max_f16 v28, v32, v28
	v_pk_max_f16 v3, v11, v3
	ds_bpermute_b32 v11, v49, v5
	v_pk_max_f16 v16, v16, v16
	v_pk_max_f16 v12, v28, v12
	s_waitcnt lgkmcnt(1)
	v_pk_add_f16 v4, v4, v10
	s_waitcnt vmcnt(2)
	ds_bpermute_b32 v10, v49, v22
	v_pk_max_f16 v20, v20, v20
	v_pk_max_f16 v12, v12, v16
	v_cndmask_b32_e32 v4, v40, v4, vcc
	v_pk_max_f16 v12, v12, v20
	v_pk_max_f16 v4, v4, v4
	s_waitcnt lgkmcnt(1)
	v_pk_add_f16 v5, v5, v11
	v_pk_max_f16 v4, v12, v4
	ds_bpermute_b32 v12, v49, v23
	v_or_b32_e32 v11, 0x180, v37
	v_cndmask_b32_e32 v5, v40, v5, vcc
	s_waitcnt lgkmcnt(1)
	v_pk_add_f16 v10, v22, v10
	v_cmp_gt_i32_e32 vcc, s4, v11
	ds_bpermute_b32 v11, v49, v24
	v_pk_max_f16 v33, v33, v33
	v_cndmask_b32_e32 v10, v40, v10, vcc
	v_pk_max_f16 v10, v10, v10
	v_pk_max_f16 v29, v29, v29
	v_pk_max_f16 v2, v2, v10
	s_waitcnt lgkmcnt(1)
	v_pk_add_f16 v10, v23, v12
	s_waitcnt lgkmcnt(0)
	v_pk_add_f16 v11, v24, v11
	v_cndmask_b32_e32 v10, v40, v10, vcc
	v_pk_max_f16 v10, v10, v10
	v_cndmask_b32_e32 v11, v40, v11, vcc
	v_pk_max_f16 v3, v3, v10
	ds_bpermute_b32 v10, v49, v25
	v_pk_max_f16 v11, v11, v11
	v_pk_max_f16 v33, v33, s3 op_sel_hi:[1,0]
	v_pk_max_f16 v4, v4, v11
	s_waitcnt vmcnt(1)
	ds_bpermute_b32 v11, v49, v6
	v_pk_max_f16 v13, v13, v13
	v_pk_max_f16 v29, v33, v29
	v_pk_max_f16 v17, v17, v17
	v_pk_max_f16 v13, v29, v13
	v_pk_max_f16 v21, v21, v21
	v_pk_max_f16 v13, v13, v17
	s_waitcnt lgkmcnt(1)
	v_pk_add_f16 v10, v25, v10
	v_pk_max_f16 v13, v13, v21
	v_pk_max_f16 v5, v5, v5
	v_cndmask_b32_e32 v10, v40, v10, vcc
	v_pk_max_f16 v5, v13, v5
	v_pk_max_f16 v10, v10, v10
	s_waitcnt lgkmcnt(0)
	v_pk_add_f16 v6, v6, v11
	ds_bpermute_b32 v11, v49, v7
	v_pk_max_f16 v5, v5, v10
	v_or_b32_e32 v10, 0x1c0, v37
	v_cmp_gt_i32_e32 vcc, s4, v10
	s_nop 1
	v_cndmask_b32_e32 v6, v40, v6, vcc
	v_pk_max_f16 v6, v6, v6
	s_nop 0
	v_pk_max_f16 v2, v2, v6
	s_waitcnt lgkmcnt(0)
	v_pk_add_f16 v6, v7, v11
	ds_bpermute_b32 v7, v49, v8
	v_cndmask_b32_e32 v6, v40, v6, vcc
	v_pk_max_f16 v6, v6, v6
	s_waitcnt lgkmcnt(0)
	v_pk_add_f16 v7, v8, v7
	v_pk_max_f16 v6, v3, v6
	ds_bpermute_b32 v3, v49, v9
	v_cndmask_b32_e32 v7, v40, v7, vcc
	v_pk_max_f16 v7, v7, v7
	s_waitcnt lgkmcnt(0)
	v_pk_add_f16 v3, v9, v3
	s_nop 0
	v_cndmask_b32_e32 v3, v40, v3, vcc
	v_pk_max_f16 v7, v4, v7
	v_pk_max_f16 v3, v3, v3
	v_and_b32_e32 v4, 64, v1
	v_pk_max_f16 v9, v5, v3
	v_xor_b32_e32 v3, 16, v1
	v_add_u32_e32 v4, 64, v4
	v_cmp_lt_i32_e32 vcc, v3, v4
	s_nop 1
	v_cndmask_b32_e32 v3, v1, v3, vcc
	v_lshlrev_b32_e32 v8, 2, v3
	ds_bpermute_b32 v5, v8, v2
	v_xor_b32_e32 v3, 32, v1
	ds_bpermute_b32 v11, v8, v6
	v_cmp_lt_i32_e32 vcc, v3, v4
	s_nop 1
	v_cndmask_b32_e32 v3, v1, v3, vcc
	v_lshlrev_b32_e32 v10, 2, v3
	s_waitcnt lgkmcnt(1)
	v_pk_max_f16 v3, v5, v5
	s_waitcnt lgkmcnt(0)
	v_pk_max_f16 v5, v11, v11
	v_pk_max_f16 v3, v2, v3
	ds_bpermute_b32 v2, v8, v7
	ds_bpermute_b32 v11, v8, v9
	v_pk_max_f16 v5, v6, v5
	ds_bpermute_b32 v4, v10, v3
	ds_bpermute_b32 v6, v10, v5
	s_waitcnt lgkmcnt(3)
	v_pk_max_f16 v2, v2, v2
	v_cmp_gt_u32_e32 vcc, 8, v38
	v_pk_max_f16 v7, v7, v2
	s_waitcnt lgkmcnt(2)
	v_pk_max_f16 v2, v11, v11
	ds_bpermute_b32 v8, v10, v7
	v_pk_max_f16 v9, v9, v2
	ds_bpermute_b32 v10, v10, v9
	v_lshlrev_b32_e32 v2, 2, v0
	s_and_saveexec_b64 s[4:5], vcc
	s_cbranch_execz .LBB2_2
	s_waitcnt lgkmcnt(0)
	v_pk_max_f16 v10, v10, v10
	v_pk_max_f16 v9, v9, v9
	v_pk_max_f16 v8, v8, v8
	v_pk_max_f16 v7, v7, v7
	v_pk_max_f16 v6, v6, v6
	v_pk_max_f16 v5, v5, v5
	v_pk_max_f16 v4, v4, v4
	v_pk_max_f16 v3, v3, v3
	v_pk_max_f16 v11, v9, v10
	v_pk_max_f16 v9, v7, v8
	v_pk_max_f16 v7, v5, v6
	v_pk_max_f16 v3, v3, v4
	v_cvt_f32_f16_e32 v6, v7
	v_cvt_f32_f16_e32 v4, v3
	v_cvt_f32_f16_sdwa v5, v3 dst_sel:DWORD dst_unused:UNUSED_PAD src0_sel:WORD_1
	v_cvt_f32_f16_sdwa v7, v7 dst_sel:DWORD dst_unused:UNUSED_PAD src0_sel:WORD_1
	v_cvt_f32_f16_e32 v8, v9
	v_cvt_f32_f16_sdwa v9, v9 dst_sel:DWORD dst_unused:UNUSED_PAD src0_sel:WORD_1
	v_cvt_f32_f16_e32 v10, v11
	v_cvt_f32_f16_sdwa v11, v11 dst_sel:DWORD dst_unused:UNUSED_PAD src0_sel:WORD_1
	v_and_b32_e32 v3, 0xf00, v2
	v_lshl_add_u32 v3, v36, 5, v3
	ds_write_b128 v3, v[4:7]
	ds_write_b128 v3, v[8:11] offset:16
